# weight-conversion loop: counted waits vmcnt(32) replace the join's vmcnt(0) so the other item's 32 loads stay in flight during each LDS transpose; with the 142/114 conversion/GEMM re-split
# speedup vs baseline: 1.0008x; 1.0008x over previous
.LBB0_413:
	s_lshl_b32 s5, s10, 6
	v_or_b32_e32 v2, s5, v37
	s_ashr_i32 s5, s5, 31
	s_mul_i32 s5, s42, s5
	v_mul_lo_u32 v39, s43, v2
	v_mad_u64_u32 v[46:47], s[48:49], s42, v2, 0
	v_add3_u32 v47, v47, s5, v39
	v_lshl_add_u64 v[46:47], v[46:47], 2, s[40:41]
	s_ashr_i32 s45, s44, 31
	v_lshl_add_u64 v[46:47], s[44:45], 2, v[46:47]
	v_lshlrev_b32_e32 v2, 2, v36
	v_lshl_add_u64 v[46:47], v[46:47], 0, v[2:3]
	s_lshl_b64 s[40:41], s[42:43], 3
	v_lshl_add_u64 v[48:49], v[46:47], 0, s[40:41]
	v_lshl_add_u64 v[50:51], v[48:49], 0, s[40:41]
	v_lshl_add_u64 v[52:53], v[50:51], 0, s[40:41]
	v_lshl_add_u64 v[54:55], v[52:53], 0, s[40:41]
	v_lshl_add_u64 v[56:57], v[54:55], 0, s[40:41]
	v_lshl_add_u64 v[58:59], v[56:57], 0, s[40:41]
	v_lshl_add_u64 v[60:61], v[58:59], 0, s[40:41]
	global_load_dword v46, v[46:47], off nt
	s_nop 0
	global_load_dword v47, v[48:49], off nt
	s_nop 0
	global_load_dword v48, v[50:51], off nt
	global_load_dword v49, v[52:53], off nt
	s_nop 0
	global_load_dword v50, v[54:55], off nt
	global_load_dword v51, v[56:57], off nt
	global_load_dword v52, v[58:59], off nt
	global_load_dword v53, v[60:61], off nt
	v_lshl_add_u64 v[56:57], v[60:61], 0, s[40:41]
	global_load_dword v54, v[56:57], off nt
	v_lshl_add_u64 v[56:57], v[56:57], 0, s[40:41]
	v_lshl_add_u64 v[58:59], v[56:57], 0, s[40:41]
	global_load_dword v55, v[56:57], off nt
	s_nop 0
	global_load_dword v56, v[58:59], off nt
	v_lshl_add_u64 v[58:59], v[58:59], 0, s[40:41]
	v_lshl_add_u64 v[60:61], v[58:59], 0, s[40:41]
	global_load_dword v57, v[58:59], off nt
	s_nop 0
	global_load_dword v58, v[60:61], off nt
	v_lshl_add_u64 v[60:61], v[60:61], 0, s[40:41]
	v_lshl_add_u64 v[62:63], v[60:61], 0, s[40:41]
	global_load_dword v59, v[60:61], off nt
	s_nop 0
	global_load_dword v60, v[62:63], off nt
	v_lshl_add_u64 v[62:63], v[62:63], 0, s[40:41]
	v_lshl_add_u64 v[64:65], v[62:63], 0, s[40:41]
	global_load_dword v61, v[62:63], off nt
	s_nop 0
	global_load_dword v62, v[64:65], off nt
	v_lshl_add_u64 v[64:65], v[64:65], 0, s[40:41]
	v_lshl_add_u64 v[66:67], v[64:65], 0, s[40:41]
	v_lshl_add_u64 v[68:69], v[66:67], 0, s[40:41]
	v_lshl_add_u64 v[70:71], v[68:69], 0, s[40:41]
	global_load_dword v63, v[64:65], off nt
	s_nop 0
	global_load_dword v64, v[66:67], off nt
	s_nop 0
	global_load_dword v66, v[68:69], off nt
	s_nop 0
	global_load_dword v68, v[70:71], off nt
	v_lshl_add_u64 v[70:71], v[70:71], 0, s[40:41]
	v_lshl_add_u64 v[72:73], v[70:71], 0, s[40:41]
	global_load_dword v69, v[70:71], off nt
	s_nop 0
	global_load_dword v70, v[72:73], off nt
	v_lshl_add_u64 v[72:73], v[72:73], 0, s[40:41]
	v_lshl_add_u64 v[74:75], v[72:73], 0, s[40:41]
	global_load_dword v71, v[72:73], off nt
	s_nop 0
	global_load_dword v72, v[74:75], off nt
	v_lshl_add_u64 v[74:75], v[74:75], 0, s[40:41]
	v_lshl_add_u64 v[76:77], v[74:75], 0, s[40:41]
	global_load_dword v73, v[74:75], off nt
	s_nop 0
	global_load_dword v74, v[76:77], off nt
	v_lshl_add_u64 v[76:77], v[76:77], 0, s[40:41]
	v_lshl_add_u64 v[78:79], v[76:77], 0, s[40:41]
	global_load_dword v75, v[76:77], off nt
	s_nop 0
	global_load_dword v76, v[78:79], off nt
	v_lshl_add_u64 v[78:79], v[78:79], 0, s[40:41]
	global_load_dword v77, v[78:79], off nt
	v_lshl_add_u64 v[78:79], v[78:79], 0, s[40:41]
	global_load_dword v67, v[78:79], off nt
	v_lshl_add_u64 v[78:79], v[78:79], 0, s[40:41]
	global_load_dword v65, v[78:79], off nt
	s_waitcnt vmcnt(32)
	s_branch .Lcv_join_a

.Lcv_join_a:
	v_add_u32_e32 v78, 0x400, v45
	v_add_u32_e32 v79, 0x800, v45
	v_add_u32_e32 v80, 0xc00, v45
	v_add_u32_e32 v81, 0x1000, v45
	v_add_u32_e32 v82, 0x1400, v45
	v_add_u32_e32 v83, 0x1800, v45
	v_add_u32_e32 v88, 0x1c00, v45
	ds_write2_b32 v45, v4, v5 offset1:66
	ds_write2_b32 v45, v6, v7 offset0:132 offset1:198
	ds_write2_b32 v78, v8, v9 offset0:8 offset1:74
	ds_write2_b32 v78, v10, v11 offset0:140 offset1:206
	ds_write2_b32 v79, v12, v13 offset0:16 offset1:82
	ds_write2_b32 v79, v14, v15 offset0:148 offset1:214
	ds_write2_b32 v80, v16, v17 offset0:24 offset1:90
	ds_write2_b32 v80, v18, v19 offset0:156 offset1:222
	ds_write2_b32 v81, v20, v21 offset0:32 offset1:98
	ds_write2_b32 v81, v22, v23 offset0:164 offset1:230
	ds_write2_b32 v82, v24, v25 offset0:40 offset1:106
	ds_write2_b32 v82, v26, v27 offset0:172 offset1:238
	ds_write2_b32 v83, v28, v29 offset0:48 offset1:114
	ds_write2_b32 v83, v30, v31 offset0:180 offset1:246
	ds_write2_b32 v88, v32, v33 offset0:56 offset1:122
	ds_write2_b32 v88, v34, v35 offset0:188 offset1:254
	v_add_u32_e32 v2, s47, v40
	s_waitcnt lgkmcnt(0)
	v_ashrrev_i32_e32 v39, 8, v2
	s_ashr_i32 s9, s8, 31
	ds_read2_b32 v[94:95], v41 offset0:33 offset1:41
	ds_read2_b32 v[96:97], v41 offset1:8
	ds_read2_b32 v[98:99], v41 offset0:66 offset1:74
	ds_read2_b32 v[100:101], v41 offset0:99 offset1:107
	ds_read2_b32 v[102:103], v41 offset0:132 offset1:140
	ds_read2_b32 v[104:105], v41 offset0:165 offset1:173
	ds_read2_b32 v[106:107], v41 offset0:198 offset1:206
	ds_read2_b32 v[108:109], v41 offset0:231 offset1:239
	v_ashrrev_i32_e32 v89, 31, v39
	s_lshl_b32 s11, s8, 8
	s_lshr_b64 s[40:41], s[8:9], 24
	s_waitcnt lgkmcnt(0)
	v_cvt_pk_bf16_f32 v90, v96, v94
	v_mul_lo_u32 v94, s40, v39
	v_mul_lo_u32 v89, s11, v89
	v_mad_u64_u32 v[110:111], s[42:43], s11, v39, 0
	v_add3_u32 v111, v111, v89, v94
	s_ashr_i32 s5, s4, 31
	v_lshl_add_u64 v[110:111], v[110:111], 1, s[6:7]
	s_lshl_b64 s[42:43], s[4:5], 15
	v_lshlrev_b32_e32 v2, 7, v2
	v_lshl_add_u64 v[110:111], v[110:111], 0, s[42:43]
	v_and_b32_e32 v2, 0x7f80, v2
	v_lshl_add_u64 v[110:111], v[110:111], 0, v[2:3]
	v_add_u32_e32 v2, s47, v42
	v_mov_b32_e32 v39, v3
	v_ashrrev_i32_e32 v89, 8, v2
	v_cvt_pk_bf16_f32 v91, v98, v100
	v_cvt_pk_bf16_f32 v92, v102, v104
	v_cvt_pk_bf16_f32 v93, v106, v108
	v_lshl_add_u64 v[110:111], v[110:111], 0, v[38:39]
	v_ashrrev_i32_e32 v94, 31, v89
	global_store_dwordx4 v[110:111], v[90:93], off nt
	v_mul_lo_u32 v96, s40, v89
	v_lshlrev_b32_e32 v2, 7, v2
	v_cvt_pk_bf16_f32 v90, v97, v95
	v_mul_lo_u32 v97, s11, v94
	v_mad_u64_u32 v[94:95], s[44:45], s11, v89, 0
	v_add3_u32 v95, v95, v97, v96
	v_lshl_add_u64 v[94:95], v[94:95], 1, s[6:7]
	v_lshl_add_u64 v[94:95], v[94:95], 0, s[42:43]
	v_and_b32_e32 v2, 0x7f80, v2
	v_lshl_add_u64 v[94:95], v[94:95], 0, v[2:3]
	v_add_u32_e32 v2, s47, v43
	v_cvt_pk_bf16_f32 v91, v99, v101
	v_cvt_pk_bf16_f32 v92, v103, v105
	v_cvt_pk_bf16_f32 v93, v107, v109
	v_lshl_add_u64 v[94:95], v[94:95], 0, v[38:39]
	v_ashrrev_i32_e32 v89, 8, v2
	ds_read2_b32 v[96:97], v41 offset0:16 offset1:24
	ds_read2_b32 v[98:99], v41 offset0:49 offset1:57
	ds_read2_b32 v[100:101], v41 offset0:82 offset1:90
	ds_read2_b32 v[102:103], v41 offset0:115 offset1:123
	ds_read2_b32 v[104:105], v41 offset0:148 offset1:156
	ds_read2_b32 v[106:107], v41 offset0:181 offset1:189
	ds_read2_b32 v[108:109], v41 offset0:214 offset1:222
	ds_read2_b32 v[110:111], v41 offset0:247 offset1:255
	global_store_dwordx4 v[94:95], v[90:93], off nt
	v_ashrrev_i32_e32 v94, 31, v89
	v_lshlrev_b32_e32 v2, 7, v2
	s_waitcnt lgkmcnt(6)
	v_cvt_pk_bf16_f32 v90, v96, v98
	v_mul_lo_u32 v96, s40, v89
	v_mul_lo_u32 v98, s11, v94
	v_mad_u64_u32 v[94:95], s[44:45], s11, v89, 0
	v_add3_u32 v95, v95, v98, v96
	v_lshl_add_u64 v[94:95], v[94:95], 1, s[6:7]
	v_lshl_add_u64 v[94:95], v[94:95], 0, s[42:43]
	v_and_b32_e32 v2, 0x7f80, v2
	v_lshl_add_u64 v[94:95], v[94:95], 0, v[2:3]
	v_add_u32_e32 v2, s47, v44
	s_waitcnt lgkmcnt(4)
	v_cvt_pk_bf16_f32 v91, v100, v102
	s_waitcnt lgkmcnt(2)
	v_cvt_pk_bf16_f32 v92, v104, v106
	s_waitcnt lgkmcnt(0)
	v_cvt_pk_bf16_f32 v93, v108, v110
	v_lshl_add_u64 v[94:95], v[94:95], 0, v[38:39]
	v_ashrrev_i32_e32 v89, 8, v2
	global_store_dwordx4 v[94:95], v[90:93], off nt
	v_ashrrev_i32_e32 v94, 31, v89
	v_mul_lo_u32 v96, s40, v89
	v_cvt_pk_bf16_f32 v90, v97, v99
	v_mul_lo_u32 v97, s11, v94
	v_mad_u64_u32 v[94:95], s[40:41], s11, v89, 0
	v_add3_u32 v95, v95, v97, v96
	v_lshl_add_u64 v[94:95], v[94:95], 1, s[6:7]
	v_lshlrev_b32_e32 v2, 7, v2
	v_lshl_add_u64 v[94:95], v[94:95], 0, s[42:43]
	v_and_b32_e32 v2, 0x7f80, v2
	v_lshl_add_u64 v[94:95], v[94:95], 0, v[2:3]
	v_cvt_pk_bf16_f32 v91, v101, v103
	v_cvt_pk_bf16_f32 v92, v105, v107
	v_cvt_pk_bf16_f32 v93, v109, v111
	v_lshl_add_u64 v[94:95], v[94:95], 0, v[38:39]
	global_store_dwordx4 v[94:95], v[90:93], off nt
	s_add_i32 s5, s33, 0x8e0
	s_waitcnt lgkmcnt(0)
	s_cmp_gt_i32 s33, 0x3691f
	s_cselect_b64 s[40:41], -1, 0
	s_and_b64 vcc, exec, s[40:41]
	s_cbranch_vccnz .LBB0_439
	s_cmpk_gt_i32 s33, 0x371f
	s_mov_b64 s[50:51], -1
	s_cbranch_scc0 .LBB0_436
	s_cmpk_gt_u32 s5, 0x4fff
	s_cbranch_scc0 .LBB0_433
	s_cmpk_gt_u32 s5, 0x51ff
	s_cbranch_scc0 .LBB0_430
	s_cmpk_gt_u32 s5, 0x61ff
	s_cbranch_scc0 .LBB0_427
	s_cmpk_gt_u32 s5, 0x71ff
	s_cbranch_scc0 .LBB0_424
	s_cmp_gt_u32 s5, 0x271ff
	s_mov_b64 s[8:9], -1
	s_cbranch_scc0 .LBB0_422
	s_add_i32 s4, s33, 0xfffd96e0
	s_lshr_b32 s34, s4, 9
	s_bfe_u32 s4, s5, 0x30006
	s_lshl_b64 s[6:7], s[34:35], 22
	v_readlane_b32 s56, v251, 0
	v_readlane_b32 s57, v251, 1
	s_add_u32 s42, s56, s6
	s_addc_u32 s43, s57, s7
	s_lshl_b64 s[6:7], s[34:35], 21
	v_readlane_b32 s8, v253, 36
	s_add_u32 s6, s8, s6
	v_readlane_b32 s8, v253, 37
	s_addc_u32 s7, s8, s7
	s_add_i32 s8, s52, 0x11c00
	v_readlane_b32 s58, v251, 2
	v_readlane_b32 s59, v251, 3
	v_readlane_b32 s60, v251, 4
	v_readlane_b32 s61, v251, 5
	v_readlane_b32 s62, v251, 6
	v_readlane_b32 s63, v251, 7
	s_and_b32 s47, s8, 0x7e0
	s_mov_b64 s[8:9], 0

.LBB0_438:
	s_lshl_b32 s9, s4, 6
	v_or_b32_e32 v2, s9, v37
	s_ashr_i32 s9, s9, 31
	s_mul_i32 s9, s44, s9
	v_mul_lo_u32 v6, s45, v2
	v_mad_u64_u32 v[4:5], s[50:51], s44, v2, 0
	v_add3_u32 v5, v5, s9, v6
	v_lshl_add_u64 v[4:5], v[4:5], 2, s[42:43]
	s_ashr_i32 s49, s48, 31
	v_lshl_add_u64 v[4:5], s[48:49], 2, v[4:5]
	v_lshlrev_b32_e32 v2, 2, v36
	v_lshl_add_u64 v[4:5], v[4:5], 0, v[2:3]
	s_lshl_b64 s[42:43], s[44:45], 3
	v_lshl_add_u64 v[6:7], v[4:5], 0, s[42:43]
	v_lshl_add_u64 v[8:9], v[6:7], 0, s[42:43]
	v_lshl_add_u64 v[10:11], v[8:9], 0, s[42:43]
	v_lshl_add_u64 v[12:13], v[10:11], 0, s[42:43]
	v_lshl_add_u64 v[14:15], v[12:13], 0, s[42:43]
	v_lshl_add_u64 v[16:17], v[14:15], 0, s[42:43]
	v_lshl_add_u64 v[18:19], v[16:17], 0, s[42:43]
	global_load_dword v4, v[4:5], off nt
	s_nop 0
	global_load_dword v5, v[6:7], off nt
	s_nop 0
	global_load_dword v6, v[8:9], off nt
	global_load_dword v7, v[10:11], off nt
	s_nop 0
	global_load_dword v8, v[12:13], off nt
	global_load_dword v9, v[14:15], off nt
	global_load_dword v10, v[16:17], off nt
	global_load_dword v11, v[18:19], off nt
	v_lshl_add_u64 v[14:15], v[18:19], 0, s[42:43]
	global_load_dword v12, v[14:15], off nt
	v_lshl_add_u64 v[14:15], v[14:15], 0, s[42:43]
	v_lshl_add_u64 v[16:17], v[14:15], 0, s[42:43]
	global_load_dword v13, v[14:15], off nt
	s_nop 0
	global_load_dword v14, v[16:17], off nt
	v_lshl_add_u64 v[16:17], v[16:17], 0, s[42:43]
	v_lshl_add_u64 v[18:19], v[16:17], 0, s[42:43]
	global_load_dword v15, v[16:17], off nt
	s_nop 0
	global_load_dword v16, v[18:19], off nt
	v_lshl_add_u64 v[18:19], v[18:19], 0, s[42:43]
	v_lshl_add_u64 v[20:21], v[18:19], 0, s[42:43]
	global_load_dword v17, v[18:19], off nt
	s_nop 0
	global_load_dword v18, v[20:21], off nt
	v_lshl_add_u64 v[20:21], v[20:21], 0, s[42:43]
	v_lshl_add_u64 v[22:23], v[20:21], 0, s[42:43]
	global_load_dword v19, v[20:21], off nt
	s_nop 0
	global_load_dword v20, v[22:23], off nt
	v_lshl_add_u64 v[22:23], v[22:23], 0, s[42:43]
	v_lshl_add_u64 v[24:25], v[22:23], 0, s[42:43]
	global_load_dword v21, v[22:23], off nt
	s_nop 0
	global_load_dword v22, v[24:25], off nt
	v_lshl_add_u64 v[24:25], v[24:25], 0, s[42:43]
	v_lshl_add_u64 v[26:27], v[24:25], 0, s[42:43]
	global_load_dword v23, v[24:25], off nt
	s_nop 0
	global_load_dword v24, v[26:27], off nt
	v_lshl_add_u64 v[26:27], v[26:27], 0, s[42:43]
	v_lshl_add_u64 v[28:29], v[26:27], 0, s[42:43]
	global_load_dword v25, v[26:27], off nt
	s_nop 0
	global_load_dword v26, v[28:29], off nt
	v_lshl_add_u64 v[28:29], v[28:29], 0, s[42:43]
	v_lshl_add_u64 v[30:31], v[28:29], 0, s[42:43]
	global_load_dword v27, v[28:29], off nt
	s_nop 0
	global_load_dword v28, v[30:31], off nt
	v_lshl_add_u64 v[30:31], v[30:31], 0, s[42:43]
	v_lshl_add_u64 v[32:33], v[30:31], 0, s[42:43]
	global_load_dword v29, v[30:31], off nt
	s_nop 0
	global_load_dword v30, v[32:33], off nt
	v_lshl_add_u64 v[32:33], v[32:33], 0, s[42:43]
	v_lshl_add_u64 v[34:35], v[32:33], 0, s[42:43]
	global_load_dword v31, v[32:33], off nt
	s_nop 0
	global_load_dword v32, v[34:35], off nt
	v_lshl_add_u64 v[34:35], v[34:35], 0, s[42:43]
	v_lshl_add_u64 v[90:91], v[34:35], 0, s[42:43]
	global_load_dword v33, v[34:35], off nt
	s_nop 0
	global_load_dword v34, v[90:91], off nt
	v_lshl_add_u64 v[90:91], v[90:91], 0, s[42:43]
	global_load_dword v35, v[90:91], off nt
	s_waitcnt vmcnt(32)
	s_branch .Lcv_join_b
.LBB0_439:
	s_waitcnt vmcnt(0)
.Lcv_join_b:
	s_andn2_b64 vcc, exec, s[38:39]
	s_cbranch_vccnz .LBB0_388
	ds_write2_b32 v45, v46, v47 offset1:66
	ds_write2_b32 v45, v48, v49 offset0:132 offset1:198
	ds_write2_b32 v78, v50, v51 offset0:8 offset1:74
	ds_write2_b32 v78, v52, v53 offset0:140 offset1:206
	ds_write2_b32 v79, v54, v55 offset0:16 offset1:82
	ds_write2_b32 v79, v56, v57 offset0:148 offset1:214
	ds_write2_b32 v80, v58, v59 offset0:24 offset1:90
	ds_write2_b32 v80, v60, v61 offset0:156 offset1:222
	ds_write2_b32 v81, v62, v63 offset0:32 offset1:98
	ds_write2_b32 v81, v64, v66 offset0:164 offset1:230
	ds_write2_b32 v82, v68, v69 offset0:40 offset1:106
	ds_write2_b32 v82, v70, v71 offset0:172 offset1:238
	ds_write2_b32 v83, v72, v73 offset0:48 offset1:114
	ds_write2_b32 v83, v74, v75 offset0:180 offset1:246
	ds_write2_b32 v88, v76, v77 offset0:56 offset1:122
	ds_write2_b32 v88, v67, v65 offset0:188 offset1:254
	s_waitcnt lgkmcnt(0)
	v_add_u32_e32 v2, s54, v40
	ds_read2_b32 v[82:83], v41 offset0:33 offset1:41
	ds_read2_b32 v[88:89], v41 offset1:8
	ds_read2_b32 v[90:91], v41 offset0:66 offset1:74
	ds_read2_b32 v[92:93], v41 offset0:99 offset1:107
	ds_read2_b32 v[94:95], v41 offset0:132 offset1:140
	ds_read2_b32 v[96:97], v41 offset0:165 offset1:173
	ds_read2_b32 v[98:99], v41 offset0:198 offset1:206
	ds_read2_b32 v[100:101], v41 offset0:231 offset1:239
	v_ashrrev_i32_e32 v39, 8, v2
	s_ashr_i32 s15, s14, 31
	s_waitcnt lgkmcnt(6)
	v_cvt_pk_bf16_f32 v78, v88, v82
	v_ashrrev_i32_e32 v82, 31, v39
	s_lshl_b32 s9, s14, 8
	s_lshr_b64 s[38:39], s[14:15], 24
	v_mul_lo_u32 v88, s38, v39
	v_mul_lo_u32 v82, s9, v82
	v_mad_u64_u32 v[102:103], s[42:43], s9, v39, 0
	v_add3_u32 v103, v103, v82, v88
	s_ashr_i32 s11, s10, 31
	v_lshl_add_u64 v[102:103], v[102:103], 1, s[12:13]
	s_lshl_b64 s[42:43], s[10:11], 15
	v_lshlrev_b32_e32 v2, 7, v2
	v_lshl_add_u64 v[102:103], v[102:103], 0, s[42:43]
	v_and_b32_e32 v2, 0x7f80, v2
	v_lshl_add_u64 v[102:103], v[102:103], 0, v[2:3]
	v_mov_b32_e32 v39, v3
	v_add_u32_e32 v2, s54, v42
	s_waitcnt lgkmcnt(4)
	v_cvt_pk_bf16_f32 v79, v90, v92
	s_waitcnt lgkmcnt(2)
	v_cvt_pk_bf16_f32 v80, v94, v96
	s_waitcnt lgkmcnt(0)
	v_cvt_pk_bf16_f32 v81, v98, v100
	v_lshl_add_u64 v[102:103], v[102:103], 0, v[38:39]
	v_ashrrev_i32_e32 v82, 8, v2
	global_store_dwordx4 v[102:103], v[78:81], off nt
	v_mul_lo_u32 v88, s38, v82
	v_lshlrev_b32_e32 v2, 7, v2
	v_cvt_pk_bf16_f32 v78, v89, v83
	v_ashrrev_i32_e32 v83, 31, v82
	v_mul_lo_u32 v89, s9, v83
	v_mad_u64_u32 v[82:83], s[44:45], s9, v82, 0
	v_add3_u32 v83, v83, v89, v88
	v_lshl_add_u64 v[82:83], v[82:83], 1, s[12:13]
	v_lshl_add_u64 v[82:83], v[82:83], 0, s[42:43]
	v_and_b32_e32 v2, 0x7f80, v2
	v_lshl_add_u64 v[82:83], v[82:83], 0, v[2:3]
	v_cvt_pk_bf16_f32 v79, v91, v93
	v_cvt_pk_bf16_f32 v80, v95, v97
	v_cvt_pk_bf16_f32 v81, v99, v101
	v_lshl_add_u64 v[82:83], v[82:83], 0, v[38:39]
	v_add_u32_e32 v2, s54, v43
	ds_read2_b32 v[88:89], v41 offset0:16 offset1:24
	ds_read2_b32 v[90:91], v41 offset0:49 offset1:57
	ds_read2_b32 v[92:93], v41 offset0:82 offset1:90
	ds_read2_b32 v[94:95], v41 offset0:115 offset1:123
	ds_read2_b32 v[96:97], v41 offset0:148 offset1:156
	ds_read2_b32 v[98:99], v41 offset0:181 offset1:189
	ds_read2_b32 v[100:101], v41 offset0:214 offset1:222
	ds_read2_b32 v[102:103], v41 offset0:247 offset1:255
	global_store_dwordx4 v[82:83], v[78:81], off nt
	v_ashrrev_i32_e32 v82, 8, v2
	v_ashrrev_i32_e32 v83, 31, v82
	s_waitcnt lgkmcnt(6)
	v_cvt_pk_bf16_f32 v78, v88, v90
	v_mul_lo_u32 v88, s38, v82
	v_mul_lo_u32 v90, s9, v83
	v_mad_u64_u32 v[82:83], s[44:45], s9, v82, 0
	v_add3_u32 v83, v83, v90, v88
	v_lshl_add_u64 v[82:83], v[82:83], 1, s[12:13]
	v_lshlrev_b32_e32 v2, 7, v2
	v_lshl_add_u64 v[82:83], v[82:83], 0, s[42:43]
	v_and_b32_e32 v2, 0x7f80, v2
	v_lshl_add_u64 v[82:83], v[82:83], 0, v[2:3]
	s_waitcnt lgkmcnt(4)
	v_cvt_pk_bf16_f32 v79, v92, v94
	s_waitcnt lgkmcnt(2)
	v_cvt_pk_bf16_f32 v80, v96, v98
	s_waitcnt lgkmcnt(0)
	v_cvt_pk_bf16_f32 v81, v100, v102
	v_lshl_add_u64 v[82:83], v[82:83], 0, v[38:39]
	v_add_u32_e32 v2, s54, v44
	global_store_dwordx4 v[82:83], v[78:81], off nt
	v_ashrrev_i32_e32 v82, 8, v2
	v_ashrrev_i32_e32 v83, 31, v82
	v_cvt_pk_bf16_f32 v78, v89, v91
	v_mul_lo_u32 v88, s38, v82
	v_mul_lo_u32 v89, s9, v83
	v_mad_u64_u32 v[82:83], s[38:39], s9, v82, 0
	v_add3_u32 v83, v83, v89, v88
	v_lshl_add_u64 v[82:83], v[82:83], 1, s[12:13]
	v_lshlrev_b32_e32 v2, 7, v2
	v_lshl_add_u64 v[82:83], v[82:83], 0, s[42:43]
	v_and_b32_e32 v2, 0x7f80, v2
	v_lshl_add_u64 v[82:83], v[82:83], 0, v[2:3]
	v_cvt_pk_bf16_f32 v79, v93, v95
	v_cvt_pk_bf16_f32 v80, v97, v99
	v_cvt_pk_bf16_f32 v81, v101, v103
	v_lshl_add_u64 v[82:83], v[82:83], 0, v[38:39]
	global_store_dwordx4 v[82:83], v[78:81], off nt
	s_waitcnt lgkmcnt(0)
	s_branch .LBB0_388
